# band attention: MFMA-to-VALU hazard pad after the QK MFMAs trimmed from 25 to 17 wait states (required: 12)
# speedup vs baseline: 1.0016x; 1.0016x over previous
; __device__ __forceinline__ void unit(LAS unsigned char* lds, const bf16* __restrict__ Q, const bf16* __restrict__ Kp, const bf16* __restrict__ VT, const float* __restrict__ rel, bf16* mix, float* ssa, int b, int h, int u) {
;     ...
;             asm volatile("s_nop 15\n\ts_nop 7" : "+v"(p0), "+v"(p1));
;             float mx = max32(p0, p1); mx = fmaxf(mx, __shfl_xor(mx, 32));
;             if (first || __any(mx > THR)) {
.LBB5_988:
	s_nop 0
	s_nop 15
	s_xor_b64 s[42:43], s[40:41], -1
	v_max3_f32 v2, v98, v99, v100
	v_max3_f32 v16, v101, v102, v103
	v_max3_f32 v17, v104, v105, v106
	v_max3_f32 v192, v107, v108, v109
	s_nop 0
	v_max3_f32 v2, v2, v110, v111
	v_max3_f32 v16, v16, v112, v113
	v_max3_f32 v17, v17, v82, v83
	v_max3_f32 v192, v192, v84, v85
	s_nop 0
	v_max3_f32 v2, v2, v86, v87
	v_max3_f32 v16, v16, v88, v89
	v_max3_f32 v17, v17, v90, v91
	v_max3_f32 v192, v192, v92, v93
	s_nop 0
	v_max3_f32 v2, v2, v94, v95
	v_max3_f32 v16, v16, v96, v97
	s_nop 0
	v_max3_f32 v2, v2, v16, v17
	s_nop 0
	v_max3_f32 v2, v2, v192, v192
	s_nop 0
	v_max_f32_e32 v2, v2, v2
	v_mov_b32_e32 v16, v2
	s_and_b64 vcc, exec, s[42:43]
	s_nop 1
	v_permlane32_swap_b32 v16, v2
	s_waitcnt lgkmcnt(0)
	v_max_f32_e32 v16, v2, v16
	s_cbranch_vccz .LBB5_1000
	v_cmp_lt_f32_e32 vcc, s17, v16
	s_mov_b64 s[46:47], 0
	s_mov_b64 s[42:43], 0
	s_cbranch_vccz .LBB5_991
	v_max_f32_e32 v2, v16, v16
	v_max_f32_e32 v2, 0, v2
	s_mov_b64 s[42:43], -1

; __device__ __forceinline__ void unit(LAS unsigned char* lds, const bf16* __restrict__ Q, const bf16* __restrict__ Kp, const bf16* __restrict__ VT, const float* __restrict__ rel, bf16* mix, float* ssa, int b, int h, int u) {
;     ...
;             asm volatile("s_nop 15\n\ts_nop 7" : "+v"(p0), "+v"(p1));
;             float mx = max32(p0, p1); mx = fmaxf(mx, __shfl_xor(mx, 32));
;             if (first || __any(mx > THR)) {
.LBB5_1024:
	s_nop 0
	s_nop 15
	s_xor_b64 s[40:41], s[38:39], -1
	v_max3_f32 v2, v98, v99, v100
	v_max3_f32 v16, v101, v102, v103
	v_max3_f32 v17, v104, v105, v106
	v_max3_f32 v189, v107, v108, v109
	s_nop 0
	v_max3_f32 v2, v2, v110, v111
	v_max3_f32 v16, v16, v112, v113
	v_max3_f32 v17, v17, v82, v83
	v_max3_f32 v189, v189, v84, v85
	s_nop 0
	v_max3_f32 v2, v2, v86, v87
	v_max3_f32 v16, v16, v88, v89
	v_max3_f32 v17, v17, v90, v91
	v_max3_f32 v189, v189, v92, v93
	s_nop 0
	v_max3_f32 v2, v2, v94, v95
	v_max3_f32 v16, v16, v96, v97
	s_nop 0
	v_max3_f32 v2, v2, v16, v17
	s_nop 0
	v_max3_f32 v2, v2, v189, v189
	s_nop 0
	v_max_f32_e32 v2, v2, v2
	v_mov_b32_e32 v16, v2
	s_and_b64 vcc, exec, s[40:41]
	s_nop 1
	v_permlane32_swap_b32 v16, v2
	s_waitcnt lgkmcnt(0)
	v_max_f32_e32 v16, v2, v16
	s_cbranch_vccz .LBB5_1036
	v_cmp_lt_f32_e32 vcc, s27, v16
	s_mov_b64 s[42:43], 0
	s_mov_b64 s[40:41], 0
	s_cbranch_vccz .LBB5_1027
	v_max_f32_e32 v2, v16, v16
	v_max_f32_e32 v2, 0, v2
	s_mov_b64 s[40:41], -1
